# MoE-down e4m3 weight conversion moved from the attention trip loop to the MoE gate/up GEMM unit epilogues (8 loads issued at epilogue start, converted and stored at its end; one item per unit per wave
# baseline (speedup 1.0000x reference)
; __global__ void __launch_bounds__(NTHREADS, 2) fwd_kernel(Args args) {
;     ...
;         const int vcu = (G % 8 == 0) ? (bx % 8) * (G / 8) + bx / 8 : bx;
;         att::CvtState cs{args.in[I_MOED], ws + W_MOED, gw * att::CV_IPW, (gw + 1) * att::CV_IPW};
;         for (int L = vcu; L < NBATCH * NH * 8; L += G) {
.LBB0_1020:
	s_or_b64 exec, exec, s[4:5]
	s_lshr_b32 s0, s3, 29
	s_add_i32 s5, s2, s0
	s_and_b32 s0, s5, -8
	s_ashr_i32 s1, s76, 3
	s_sub_i32 s0, s2, s0
	s_mul_i32 s8, s1, s0
	s_ashr_i32 s1, s5, 3
	s_and_b32 s4, s76, 7
	s_add_i32 s5, s8, s1
	v_readlane_b32 s8, v251, 9
	s_add_u32 s30, s70, 0x24a00000
	s_mul_i32 s35, s8, 28
	s_addc_u32 s31, s71, 0
	s_mov_b32 s50, s35
	v_readlane_b32 s9, v251, 10
	s_add_u32 s8, s70, 0x4bc00000
	s_addc_u32 s9, s71, 0
	s_cmp_eq_u32 s4, 0
	s_cselect_b32 s51, s5, s2
	s_cmpk_gt_i32 s51, 0x1ff
	s_waitcnt lgkmcnt(0)
	s_barrier
	s_cbranch_scc1 .LBB0_1053
	s_add_u32 s4, s70, 0x3da00000
	s_addc_u32 s5, s71, 0
	s_add_u32 s10, s70, 0x3c200000
	s_addc_u32 s11, s71, 0
	s_movk_i32 s52, 0x2000
	s_mov_b32 s53, 0xc3e00000
	v_mov_b32_e32 v203, 0x43e00000
	v_mov_b32_e32 v191, 0
	s_movk_i32 s54, 0xd0
	s_movk_i32 s55, 0x3000
	s_mov_b32 s56, 0x5010400
	s_mov_b32 s57, 0x7030602
	s_mov_b32 s58, 0x5040100
	s_mov_b32 s59, 0x7060302
	s_add_i32 s60, 0, 0x6800
	s_movk_i32 s61, 0x1c00
	s_movk_i32 s62, 0x4000
	s_movk_i32 s63, 0x6000
	s_mov_b32 s64, 0x8000
	s_mov_b32 s65, 0xa000
	s_mov_b32 s66, 0xc000
	s_mov_b32 s67, 0xe000
	v_mov_b32_e32 v208, 0x1c00
	v_mov_b32_e32 v209, 0xff800000
	v_readlane_b32 s18, v251, 0
	v_readlane_b32 s19, v251, 1
	v_readlane_b32 s98, v251, 9
	s_nop 3
	s_sub_u32 s18, s18, 0x38
	s_subb_u32 s19, s19, 0
	s_load_dwordx4 s[44:47], s[18:19], 0x0
	s_mul_i32 s98, s98, 28
	s_add_i32 s99, s98, 28
	s_mov_b32 s100, 0
	s_waitcnt lgkmcnt(0)
	v_writelane_b32 v252, s44, 0
	v_writelane_b32 v252, s45, 1
	v_writelane_b32 v252, s46, 2
	v_writelane_b32 v252, s47, 3
	s_branch .LBB0_1023

; #define PG8_WAIT_V(n) asm volatile("s_waitcnt vmcnt(" #n ")" ::: "memory")
;     ...
;     const int tid = opaque_tid(), wid = __builtin_amdgcn_readfirstlane(tid >> 6), lane = tid & 63, wr = wid >> 2, wc = wid & 3, fr = lane & 15, fq = lane >> 4;
;     const int K = g.K, nt = K / 128;
;     unsigned voffA[2], voffB[2];
; #pragma unroll
;     for (int i = 0; i < 2; ++i) { int R, C; stage_rc8(tid * 16 + i * 8192, R, C); const int Rb = Epi::PERM ? ((R & ~31) + perm32(R & 31)) : R;
;         voffA[i] = (unsigned)(R * g.lda + C); voffB[i] = (unsigned)(Rb * g.ldb + C); }
;     const size_t kstep = 128;
;     const size_t hstepA = (size_t)HALF * g.lda, hstepB = (size_t)HALF * g.ldb;
;     const unsigned ldsw = (unsigned)wid * 1024u;
;     const int aoff0 = lds_byte8(wr * 64 + fr, 2 * fq), aoff1 = lds_byte8(wr * 64 + fr, 2 * fq + 1), boff0 = lds_byte8(wc * 32 + fr, 2 * fq), boff1 = lds_byte8(wc * 32 + fr, 2 * fq + 1);
;     ...
;     Unit cur, nxt; int ui = 0;
;     if (!S.next(0, cur)) return;
;     Acc acc;
; #pragma unroll
;     for (int a = 0; a < 2; ++a)
; #pragma unroll
;         for (int b = 0; b < 2; ++b)
; #pragma unroll
;             for (int m = 0; m < 4; ++m)
; #pragma unroll
;                 for (int n = 0; n < 2; ++n) acc[a][b][m][n] = (f32x4){0.f, 0.f, 0.f, 0.f};
;     typename Frag8<FP6>::T At[4], B0[2], B1[2];
;     const char* cA = (const char*)g.A + cur.aoff; const char* cB = (const char*)g.Bt + cur.boff;
;     S.a_ready(cur);
;     PG8_STAGE(PG8_SB(0, 0), cB, voffB); PG8_STAGE(PG8_SB(0, 1), cB + hstepB, voffB); PG8_STAGE(PG8_SA(0, 0), cA, voffA); PG8_STAGE(PG8_SA(0, 1), cA + hstepA, voffA);
;     if (wr == 1) PG8_BAR;
;     PG8_WAIT_V(2); PG8_BAR;
; __device__ __forceinline__ void cvt_load(const CvtState& cs, int lane, f32x4 (&v)[8]) {
;     const int kb = cs.next % CV_KB, tmp = cs.next / CV_KB, nb = tmp % CV_NB, e = tmp / CV_NB;
;     const float* src = cs.W + ((size_t)e * FF + (size_t)(128 * kb + 8 * (lane >> 2))) * D + 16 * nb + 4 * (lane & 3);
; #pragma unroll
;     for (int i = 0; i < 8; ++i) v[i] = *(const f32x4*)(src + (size_t)i * D);
; }
; __device__ __forceinline__ void cvt_store(CvtState& cs, int lane, const f32x4 (&v)[8]) {
;     const int kb = cs.next % CV_KB, tmp = cs.next / CV_KB, nb = tmp % CV_NB, e = tmp / CV_NB;
;     unsigned char* dst = cs.WT + ((size_t)e * D + (size_t)(16 * nb + 4 * (lane & 3))) * FF + 128 * kb + 8 * (lane >> 2);
.LBB0_1400:
	s_or_b64 exec, exec, s[4:5]
	v_readlane_b32 s98, v251, 9
	v_readlane_b32 s100, v251, 0
	v_readlane_b32 s101, v251, 1
	v_mbcnt_lo_u32_b32 v244, -1, 0
	v_mbcnt_hi_u32_b32 v244, -1, v244
	s_nop 3
	s_sub_u32 s100, s100, 0x28
	s_subb_u32 s101, s101, 0
	s_load_dwordx2 s[100:101], s[100:101], 0x0
	s_lshr_b32 s4, s98, 8
	s_lshr_b32 s5, s98, 1
	s_and_b32 s5, s5, 0x7f
	s_and_b32 s8, s98, 1
	s_mul_i32 s8, s8, 0xe00
	s_mul_i32 s9, s4, 0x1c00
	s_add_u32 s9, s9, s8
	s_lshl_b32 s9, s9, 13
	s_lshl_b32 s12, s5, 6
	s_add_u32 s9, s9, s12
	s_lshl_b32 s12, s4, 11
	s_lshl_b32 s13, s5, 4
	s_add_u32 s12, s12, s13
	s_mul_i32 s12, s12, 0x1c00
	s_add_u32 s12, s12, s8
	v_lshrrev_b32_e32 v245, 2, v244
	v_and_b32_e32 v246, 3, v244
	v_lshlrev_b32_e32 v247, 16, v245
	v_lshl_add_u32 v247, v246, 4, v247
	v_mul_u32_u24_e32 v246, 0x7000, v246
	v_lshl_add_u32 v246, v245, 3, v246
	v_add_u32_e32 v247, s9, v247
	v_add_u32_e32 v246, s12, v246
	s_add_u32 s4, s70, 0x24a00000
	s_addc_u32 s5, s71, 0
	s_waitcnt lgkmcnt(0)
	v_mov_b32_e32 v244, s100
	v_mov_b32_e32 v245, s101
	v_add_co_u32_e32 v244, vcc, v244, v247
	s_nop 1
	v_addc_co_u32_e32 v245, vcc, 0, v245, vcc
	v_mov_b32_e32 v247, s5
	v_add_co_u32_e32 v246, vcc, s4, v246
	s_nop 1
	v_addc_co_u32_e32 v247, vcc, 0, v247, vcc
	v_mov_b32_e32 v248, 0x43e00000
	v_mov_b32_e32 v249, 0xc3e00000
	s_mov_b32 s98, 0
	s_mov_b32 s99, 0
	s_mov_b32 s100, 0
	s_mov_b32 s101, 0
	s_add_u32 s8, s70, 0x3f200000
	s_addc_u32 s9, s71, 0
	s_cmp_lt_i32 s0, 0
	s_cselect_b64 s[12:13], -1, 0
	s_add_i32 s4, 0, 0x217fc
	v_mov_b32_e32 v1, s4
	s_waitcnt lgkmcnt(0)
	s_barrier
	ds_read_b32 v1, v1
	v_mov_b32_e32 v12, v0
	s_waitcnt lgkmcnt(0)
	v_mul_lo_u32 v154, v1, 56
	v_cmp_ge_i32_e32 vcc, s2, v154
	v_readfirstlane_b32 s24, v1
	v_readfirstlane_b32 s4, v12
	s_cbranch_vccnz .LBB0_1416
	v_lshlrev_b32_e32 v1, 4, v12
	v_add_u32_e32 v2, 0x2000, v1
	s_ashr_i32 s16, s4, 6
	v_ashrrev_i32_e32 v10, 7, v2
	v_bfe_u32 v4, v2, 7, 2
	s_mov_b32 s14, 0x1fffe0
	s_mul_i32 s25, s24, 7
	s_ashr_i32 s5, s4, 8
	s_lshl_b32 s17, s16, 10
	v_and_or_b32 v4, v10, s14, v4
	v_bfe_u32 v11, v2, 7, 4
	s_mov_b32 s14, 0x1ffff0
	v_ashrrev_i32_e32 v13, 3, v12
	v_bfe_u32 v14, v1, 7, 4
	s_add_i32 s33, s25, 1
	v_and_or_b32 v6, v10, s14, v11
	v_and_or_b32 v7, v13, s14, v14
	s_and_b64 s[14:15], s[12:13], exec
	s_cselect_b32 s14, s33, s25
	s_mul_i32 s14, s14, s0
	s_add_i32 s14, s14, s1
	v_lshrrev_b32_e32 v3, 7, v2
	v_lshrrev_b32_e32 v5, 2, v10
	v_lshrrev_b32_e32 v2, 6, v2
	s_mul_hi_i32 s15, s14, 0x92492493
	v_and_b32_e32 v5, 4, v5
	v_and_b32_e32 v2, 24, v2
	s_add_i32 s15, s15, s14
	v_or3_b32 v2, v4, v5, v2
	v_bfe_u32 v4, v3, 3, 1
	s_lshr_b32 s18, s15, 31
	s_ashr_i32 s15, s15, 8
	v_and_or_b32 v3, v3, 6, v4
	s_add_i32 s15, s15, s18
	v_lshlrev_b32_e32 v2, 11, v2
	v_lshlrev_b32_e32 v3, 4, v3
	v_and_b32_e32 v4, 0x70, v1
	s_lshl_b32 s18, s15, 3
	v_bitop3_b32 v156, v2, v3, v4 bitop3:0xf6
	v_lshlrev_b32_e32 v2, 11, v6
	s_sub_i32 s19, s24, s18
	v_bitop3_b32 v158, v3, v2, v4 bitop3:0xde
	v_bfe_u32 v2, v12, 3, 25
	v_and_b32_e32 v5, 0x1fffe0, v13
	v_lshrrev_b32_e32 v6, 2, v13
	v_lshrrev_b32_e32 v8, 2, v12
	s_min_i32 s19, s19, 8
	v_and_or_b32 v5, v2, 3, v5
	v_and_b32_e32 v6, 4, v6
	v_and_b32_e32 v8, 24, v8
	s_abs_i32 s20, s19
	v_or3_b32 v5, v5, v6, v8
	v_cvt_f32_u32_e32 v6, s20
	s_sub_i32 s22, 0, s20
	s_mulk_i32 s15, 0x1c0
	s_sub_i32 s14, s14, s15
	v_rcp_iflag_f32_e32 v6, v6
	s_abs_i32 s21, s14
	s_xor_b32 s15, s14, s19
	s_ashr_i32 s15, s15, 31
	v_mul_f32_e32 v6, 0x4f7ffffe, v6
	v_cvt_u32_f32_e32 v6, v6
	v_bfe_u32 v8, v2, 3, 1
	v_and_or_b32 v2, v2, 6, v8
	v_lshlrev_b32_e32 v5, 11, v5
	v_readfirstlane_b32 s23, v6
	s_mul_i32 s22, s22, s23
	s_mul_hi_u32 s22, s23, s22
	s_add_i32 s23, s23, s22
	s_mul_hi_u32 s22, s21, s23
	s_mul_i32 s23, s22, s20
	s_sub_i32 s21, s21, s23
	s_add_i32 s23, s22, 1
	s_sub_i32 s26, s21, s20
	s_cmp_ge_u32 s21, s20
	s_cselect_b32 s22, s23, s22
	s_cselect_b32 s21, s26, s21
	s_add_i32 s23, s22, 1
	s_cmp_ge_u32 s21, s20
	s_cselect_b32 s20, s23, s22
	s_xor_b32 s20, s20, s15
	s_sub_i32 s67, s20, s15
	s_mul_i32 s15, s67, s19
	s_sub_i32 s14, s14, s15
	s_add_i32 s42, s18, s14
	s_lshl_b32 s14, s42, 2
	s_add_i32 s14, s14, 0
	s_add_i32 s14, s14, 0x21400
	v_mov_b32_e32 v6, s14
	ds_read_b32 v6, v6
	s_ashr_i32 s15, s67, 31
	v_readlane_b32 s20, v251, 46
	v_lshlrev_b32_e32 v2, 4, v2
	v_bitop3_b32 v160, v5, v2, v4 bitop3:0xf6
	s_waitcnt lgkmcnt(0)
	v_readfirstlane_b32 s14, v6
	s_and_b32 s14, s14, 7
	s_mul_i32 s14, s14, 56
	s_add_u32 s14, s14, s67
	s_addc_u32 s15, 0, s15
	s_ashr_i32 s43, s42, 31
	s_lshl_b64 s[14:15], s[14:15], 19
	s_lshl_b64 s[18:19], s[42:43], 19
	s_add_u32 s46, s20, s14
	v_readlane_b32 s14, v251, 45
	s_addc_u32 s47, s14, s15
	s_add_i32 s35, s17, 0
	s_add_i32 s43, s35, 0x10000
	s_add_i32 s52, s35, 0x12000
	s_mov_b32 m0, s43
	s_add_u32 s14, s46, 0x40000
	global_load_lds_dwordx4 v160, s[46:47]
	s_mov_b32 m0, s52
	s_addc_u32 s15, s47, 0
	s_add_i32 s53, s35, 0x14000
	s_add_i32 s54, s35, 0x16000
	global_load_lds_dwordx4 v156, s[46:47]
	s_mov_b32 m0, s53
	s_add_u32 s44, s36, s18
	v_lshlrev_b32_e32 v5, 11, v7
	global_load_lds_dwordx4 v160, s[14:15]
	s_mov_b32 m0, s54
	s_addc_u32 s45, s37, s19
	s_add_i32 s55, s35, 0x2000
	v_bitop3_b32 v162, v2, v5, v4 bitop3:0xde
	global_load_lds_dwordx4 v156, s[14:15]
	s_mov_b32 m0, s35
	s_add_u32 s14, s44, 0x40000
	global_load_lds_dwordx4 v162, s[44:45]
	s_mov_b32 m0, s55
	s_addc_u32 s15, s45, 0
	s_add_i32 s56, s35, 0x4000
	global_load_lds_dwordx4 v158, s[44:45]
	s_mov_b32 m0, s56
	s_add_i32 s57, s35, 0x6000
	global_load_lds_dwordx4 v162, s[14:15]
	s_mov_b32 m0, s57
	v_mov_b32_e32 v161, 0
	global_load_lds_dwordx4 v158, s[14:15]
	s_movk_i32 s14, 0x70
	v_mov_b32_e32 v157, v161
	v_mov_b32_e32 v163, v161
	v_mov_b32_e32 v159, v161
	s_cmp_eq_u32 s5, 1
	v_bitop3_b32 v15, v3, v1, s14 bitop3:0x78
	v_bitop3_b32 v16, v2, v1, s14 bitop3:0x78
	v_lshl_add_u64 v[8:9], s[46:47], 0, v[160:161]
	v_lshl_add_u64 v[6:7], s[46:47], 0, v[156:157]
	v_lshl_add_u64 v[2:3], s[44:45], 0, v[162:163]
	s_cselect_b64 s[14:15], -1, 0
	s_cmp_lg_u32 s5, 1
	v_lshl_add_u64 v[4:5], s[44:45], 0, v[158:159]
	s_cbranch_scc1 .LBB0_1403
	s_barrier

;     __device__ __forceinline__ bool next(int i, Unit& u) const { if (!T.tile(i, u.pm, u.pn)) return false; u.aoff = (size_t)u.pm * atile; u.boff = (size_t)u.pn * btile; return true; }
;     __device__ __forceinline__ bool next(int i, Unit& u) const { if (!T.tile(i, u.pm, u.pn)) return false; u.aoff = (size_t)u.pm * 256 * D * 2 + (size_t)(u.pn >> 1) * 512; u.boff = (size_t)u.pn * 256 * 256 * 2; return true; }
;     __device__ __forceinline__ bool next(int i, Unit& u) const { if (!T.tile(i, u.pm, u.pn)) return false; const int e = tile_e[u.pm] & 7; u.aoff = (size_t)u.pm * atile; u.boff = ((size_t)e * nN + u.pn) * btile; return true; }
;     __device__ __forceinline__ void operator()(const Acc& acc, const Unit& u, int wr, int wc, int fr, int fq) const {
;         const int row0 = u.pm * BM + wr * 64 + fr, col0 = u.pn * HALF + wc * 32 + 8 * fq;
;         const float k_ = in_scale * in_scale * out_scale, c1 = -in_scale * 1.4426950408889634f, c0 = -__builtin_log2f(k_), c3 = 1.0f / k_;
; #pragma unroll
;         for (int ai = 0; ai < 2; ++ai)
; #pragma unroll
;             for (int m = 0; m < 4; ++m) { const size_t off = (size_t)(row0 + ai * HALF + m * 16) * ldc + col0;
;                 float h[8];
; #pragma unroll
;                 for (int n = 0; n < 2; ++n)
; #pragma unroll
;                     for (int e = 0; e < 4; ++e) { const float a0 = acc[ai][0][m][n][e], a1 = acc[ai][1][m][n][e];
;                         h[n * 4 + e] = (a0 * a1) * __builtin_amdgcn_rcpf(c3 + __builtin_amdgcn_exp2f(fmaf(a0, c1, c0))); }
;                 if constexpr (FP8OUT == 2) { u32x2 w; w.x = pk4_i8(h[0], h[1], h[2], h[3]); w.y = pk4_i8(h[4], h[5], h[6], h[7]); *(u32x2*)((unsigned char*)H + off) = w; }
;                 else if constexpr (FP8OUT == 1) { u32x2 w; w.x = pk4_fp8_nc(h[0], h[1], h[2], h[3]); w.y = pk4_fp8_nc(h[4], h[5], h[6], h[7]); *(u32x2*)((unsigned char*)H + off) = w; }
; __device__ __forceinline__ void cvt_load(const CvtState& cs, int lane, f32x4 (&v)[8]) {
;     const int kb = cs.next % CV_KB, tmp = cs.next / CV_KB, nb = tmp % CV_NB, e = tmp / CV_NB;
;     const float* src = cs.W + ((size_t)e * FF + (size_t)(128 * kb + 8 * (lane >> 2))) * D + 16 * nb + 4 * (lane & 3);
; #pragma unroll
;     for (int i = 0; i < 8; ++i) v[i] = *(const f32x4*)(src + (size_t)i * D);
; }
.LBB0_1412:
	s_cmp_lt_u32 s98, 28
	s_cbranch_scc0 .Lmd_noload
	s_lshl_b32 s100, s98, 20
	v_lshl_add_u64 v[234:235], s[100:101], 0, v[244:245]
	global_load_dwordx4 v[202:205], v[234:235], off
	s_mov_b32 s100, 0x2000
	v_lshl_add_u64 v[236:237], s[100:101], 0, v[234:235]
	global_load_dwordx4 v[206:209], v[236:237], off
	s_mov_b32 s100, 0x4000
	v_lshl_add_u64 v[236:237], s[100:101], 0, v[234:235]
	global_load_dwordx4 v[210:213], v[236:237], off
	s_mov_b32 s100, 0x6000
	v_lshl_add_u64 v[236:237], s[100:101], 0, v[234:235]
	global_load_dwordx4 v[214:217], v[236:237], off
	s_mov_b32 s100, 0x8000
	v_lshl_add_u64 v[236:237], s[100:101], 0, v[234:235]
	global_load_dwordx4 v[218:221], v[236:237], off
	s_mov_b32 s100, 0xa000
	v_lshl_add_u64 v[236:237], s[100:101], 0, v[234:235]
	global_load_dwordx4 v[222:225], v[236:237], off
	s_mov_b32 s100, 0xc000
	v_lshl_add_u64 v[236:237], s[100:101], 0, v[234:235]
	global_load_dwordx4 v[226:229], v[236:237], off
	s_mov_b32 s100, 0xe000
	v_lshl_add_u64 v[236:237], s[100:101], 0, v[234:235]
	global_load_dwordx4 v[230:233], v[236:237], off
.Lmd_noload:
	v_fmamk_f32 v2, v150, 0xbc03513b, v201
	v_exp_f32_e32 v3, v2
	v_fmamk_f32 v4, v151, 0xbc03513b, v201
	v_mul_f32_e32 v7, v150, v146
	v_exp_f32_e32 v4, v4
	v_add_f32_e32 v3, 0x45fd2000, v3
	v_rcp_f32_e32 v5, v3
	v_fmamk_f32 v9, v153, 0xbc03513b, v201
	v_add_f32_e32 v4, 0x45fd2000, v4
	v_rcp_f32_e32 v4, v4
	v_mul_f32_e32 v5, v5, v7
	v_fmamk_f32 v7, v152, 0xbc03513b, v201
	v_exp_f32_e32 v7, v7
	v_exp_f32_e32 v9, v9
	v_fmamk_f32 v10, v142, 0xbc03513b, v201
	v_exp_f32_e32 v10, v10
	v_add_f32_e32 v7, 0x45fd2000, v7
	v_rcp_f32_e32 v7, v7
	v_mul_f32_e32 v8, v151, v147
	v_mul_f32_e32 v4, v4, v8
	v_mul_f32_e32 v8, v152, v148
	v_mul_f32_e32 v7, v7, v8
	v_add_f32_e32 v8, 0x45fd2000, v9
	v_rcp_f32_e32 v8, v8
	v_add_f32_e32 v9, 0x45fd2000, v10
	v_rcp_f32_e32 v9, v9
	v_mul_f32_e32 v10, v153, v149
	v_mul_f32_e32 v10, v8, v10
	v_mul_f32_e32 v8, v142, v138
	v_mul_f32_e32 v11, v9, v8
	v_fmamk_f32 v8, v143, 0xbc03513b, v201
	v_exp_f32_e32 v8, v8
	v_fmamk_f32 v9, v144, 0xbc03513b, v201
	v_exp_f32_e32 v9, v9
	v_fmamk_f32 v13, v145, 0xbc03513b, v201
	v_add_f32_e32 v8, 0x45fd2000, v8
	v_rcp_f32_e32 v8, v8
	v_add_f32_e32 v9, 0x45fd2000, v9
	v_rcp_f32_e32 v9, v9
	v_exp_f32_e32 v13, v13
	v_mul_f32_e32 v12, v143, v139
	v_mul_f32_e32 v12, v8, v12
	v_mul_f32_e32 v8, v144, v140
	v_mul_f32_e32 v14, v9, v8
	v_add_f32_e32 v8, 0x45fd2000, v13
	v_rcp_f32_e32 v13, v8
	v_mov_b32_e32 v8, 0
	v_cvt_pk_fp8_f32 v8, v5, v4
	v_mov_b32_e32 v9, 0
	v_cvt_pk_fp8_f32 v9, v11, v12
	v_mul_f32_e32 v4, v145, v141
	v_cvt_pk_fp8_f32 v8, v7, v10 op_sel:[0,0,1]
	v_fmamk_f32 v7, v134, 0xbc03513b, v201
	v_exp_f32_e32 v7, v7
	v_mul_f32_e32 v4, v13, v4
	v_cvt_pk_fp8_f32 v9, v14, v4 op_sel:[0,0,1]
	v_lshl_add_u32 v6, s42, 8, v1
	v_add_f32_e32 v7, 0x45fd2000, v7
	v_lshl_or_b32 v2, s67, 7, v198
	v_mov_b64_e32 v[4:5], s[8:9]
	v_rcp_f32_e32 v7, v7
	v_ashrrev_i32_e32 v3, 31, v2
	v_mad_i64_i32 v[10:11], s[44:45], v6, s65, v[4:5]
	v_lshl_add_u64 v[10:11], v[10:11], 0, v[2:3]
	global_store_dwordx2 v[10:11], v[8:9], off
	v_fmamk_f32 v8, v135, 0xbc03513b, v201
	v_mul_f32_e32 v9, v134, v130
	v_exp_f32_e32 v8, v8
	v_mul_f32_e32 v7, v7, v9
	v_fmamk_f32 v9, v136, 0xbc03513b, v201
	v_exp_f32_e32 v9, v9
	v_add_f32_e32 v8, 0x45fd2000, v8
	v_rcp_f32_e32 v8, v8
	v_fmamk_f32 v12, v137, 0xbc03513b, v201
	v_add_f32_e32 v9, 0x45fd2000, v9
	v_rcp_f32_e32 v9, v9
	v_exp_f32_e32 v12, v12
	v_fmamk_f32 v13, v126, 0xbc03513b, v201
	v_exp_f32_e32 v13, v13
	v_mul_f32_e32 v11, v135, v131
	v_mul_f32_e32 v11, v8, v11
	v_mul_f32_e32 v8, v136, v132
	v_mul_f32_e32 v14, v9, v8
	v_add_f32_e32 v8, 0x45fd2000, v12
	v_rcp_f32_e32 v8, v8
	v_add_f32_e32 v9, 0x45fd2000, v13
	v_rcp_f32_e32 v9, v9
	v_mul_f32_e32 v12, v137, v133
	v_mul_f32_e32 v12, v8, v12
	v_mul_f32_e32 v8, v126, v122
	v_mul_f32_e32 v13, v9, v8
	v_fmamk_f32 v8, v127, 0xbc03513b, v201
	v_exp_f32_e32 v8, v8
	v_fmamk_f32 v9, v128, 0xbc03513b, v201
	v_exp_f32_e32 v9, v9
	v_fmamk_f32 v16, v129, 0xbc03513b, v201
	v_add_f32_e32 v8, 0x45fd2000, v8
	v_rcp_f32_e32 v8, v8
	v_add_f32_e32 v9, 0x45fd2000, v9
	v_rcp_f32_e32 v9, v9
	v_exp_f32_e32 v16, v16
	v_mul_f32_e32 v15, v127, v123
	v_mul_f32_e32 v15, v8, v15
	v_mul_f32_e32 v8, v128, v124
	v_mul_f32_e32 v17, v9, v8
	v_add_f32_e32 v8, 0x45fd2000, v16
	v_rcp_f32_e32 v16, v8
	v_mov_b32_e32 v9, 0
	v_cvt_pk_fp8_f32 v9, v13, v15
	v_mov_b32_e32 v8, 0
	v_cvt_pk_fp8_f32 v8, v7, v11
	v_mul_f32_e32 v7, v129, v125
	v_mul_f32_e32 v7, v16, v7
	v_cvt_pk_fp8_f32 v9, v17, v7 op_sel:[0,0,1]
	v_fmamk_f32 v7, v118, 0xbc03513b, v201
	v_exp_f32_e32 v7, v7
	v_cvt_pk_fp8_f32 v8, v14, v12 op_sel:[0,0,1]
	v_or_b32_e32 v10, 16, v6
	v_mad_i64_i32 v[10:11], s[44:45], v10, s65, v[4:5]
	v_add_f32_e32 v7, 0x45fd2000, v7
	v_rcp_f32_e32 v7, v7
	v_lshl_add_u64 v[10:11], v[10:11], 0, v[2:3]
	global_store_dwordx2 v[10:11], v[8:9], off
	v_fmamk_f32 v8, v119, 0xbc03513b, v201
	v_mul_f32_e32 v9, v118, v114
	v_exp_f32_e32 v8, v8
	v_mul_f32_e32 v7, v7, v9
	v_fmamk_f32 v9, v120, 0xbc03513b, v201
	v_exp_f32_e32 v9, v9
	v_add_f32_e32 v8, 0x45fd2000, v8
	v_rcp_f32_e32 v8, v8
	v_fmamk_f32 v12, v121, 0xbc03513b, v201
	v_add_f32_e32 v9, 0x45fd2000, v9
	v_rcp_f32_e32 v9, v9
	v_exp_f32_e32 v12, v12
	v_fmamk_f32 v13, v110, 0xbc03513b, v201
	v_exp_f32_e32 v13, v13
	v_mul_f32_e32 v11, v119, v115
	v_mul_f32_e32 v11, v8, v11
	v_mul_f32_e32 v8, v120, v116
	v_mul_f32_e32 v14, v9, v8
	v_add_f32_e32 v8, 0x45fd2000, v12
	v_rcp_f32_e32 v8, v8
	v_add_f32_e32 v9, 0x45fd2000, v13
	v_rcp_f32_e32 v9, v9
	v_mul_f32_e32 v12, v121, v117
	v_mul_f32_e32 v12, v8, v12
	v_mul_f32_e32 v8, v110, v106
	v_mul_f32_e32 v13, v9, v8
;     __device__ __forceinline__ void operator()(const Acc& acc, const Unit& u, int wr, int wc, int fr, int fq) const {
;     ...
;         for (int ai = 0; ai < 2; ++ai)
; #pragma unroll
;             for (int m = 0; m < 4; ++m) { const size_t off = (size_t)(row0 + ai * HALF + m * 16) * ldc + col0;
;                 float h[8];
; #pragma unroll
;                 for (int n = 0; n < 2; ++n)
; #pragma unroll
;                     for (int e = 0; e < 4; ++e) { const float a0 = acc[ai][0][m][n][e], a1 = acc[ai][1][m][n][e];
;                         h[n * 4 + e] = (a0 * a1) * __builtin_amdgcn_rcpf(c3 + __builtin_amdgcn_exp2f(fmaf(a0, c1, c0))); }
;                 if constexpr (FP8OUT == 2) { u32x2 w; w.x = pk4_i8(h[0], h[1], h[2], h[3]); w.y = pk4_i8(h[4], h[5], h[6], h[7]); *(u32x2*)((unsigned char*)H + off) = w; }
;                 else if constexpr (FP8OUT == 1) { u32x2 w; w.x = pk4_fp8_nc(h[0], h[1], h[2], h[3]); w.y = pk4_fp8_nc(h[4], h[5], h[6], h[7]); *(u32x2*)((unsigned char*)H + off) = w; }
	v_fmamk_f32 v8, v111, 0xbc03513b, v201
	v_exp_f32_e32 v8, v8
	v_fmamk_f32 v9, v112, 0xbc03513b, v201
	v_exp_f32_e32 v9, v9
	v_fmamk_f32 v16, v113, 0xbc03513b, v201
	v_add_f32_e32 v8, 0x45fd2000, v8
	v_rcp_f32_e32 v8, v8
	v_add_f32_e32 v9, 0x45fd2000, v9
	v_rcp_f32_e32 v9, v9
	v_exp_f32_e32 v16, v16
	v_mul_f32_e32 v15, v111, v107
	v_mul_f32_e32 v15, v8, v15
	v_mul_f32_e32 v8, v112, v108
	v_mul_f32_e32 v17, v9, v8
	v_add_f32_e32 v8, 0x45fd2000, v16
	v_rcp_f32_e32 v16, v8
	v_mov_b32_e32 v9, 0
	v_cvt_pk_fp8_f32 v9, v13, v15
	v_mov_b32_e32 v8, 0
	v_cvt_pk_fp8_f32 v8, v7, v11
	v_mul_f32_e32 v7, v113, v109
	v_mul_f32_e32 v7, v16, v7
	v_cvt_pk_fp8_f32 v9, v17, v7 op_sel:[0,0,1]
	v_fmamk_f32 v7, v102, 0xbc03513b, v201
	v_exp_f32_e32 v7, v7
	v_cvt_pk_fp8_f32 v8, v14, v12 op_sel:[0,0,1]
	v_or_b32_e32 v10, 32, v6
	v_mad_i64_i32 v[10:11], s[44:45], v10, s65, v[4:5]
	v_add_f32_e32 v7, 0x45fd2000, v7
	v_rcp_f32_e32 v7, v7
	v_lshl_add_u64 v[10:11], v[10:11], 0, v[2:3]
	global_store_dwordx2 v[10:11], v[8:9], off
	v_fmamk_f32 v8, v103, 0xbc03513b, v201
	v_mul_f32_e32 v9, v102, v98
	v_exp_f32_e32 v8, v8
	v_mul_f32_e32 v7, v7, v9
	v_fmamk_f32 v9, v104, 0xbc03513b, v201
	v_exp_f32_e32 v9, v9
	v_add_f32_e32 v8, 0x45fd2000, v8
	v_rcp_f32_e32 v8, v8
	v_fmamk_f32 v12, v105, 0xbc03513b, v201
	v_add_f32_e32 v9, 0x45fd2000, v9
	v_rcp_f32_e32 v9, v9
	v_exp_f32_e32 v12, v12
	v_fmamk_f32 v13, v94, 0xbc03513b, v201
	v_exp_f32_e32 v13, v13
	v_mul_f32_e32 v11, v103, v99
	v_mul_f32_e32 v11, v8, v11
	v_mul_f32_e32 v8, v104, v100
	v_mul_f32_e32 v14, v9, v8
	v_add_f32_e32 v8, 0x45fd2000, v12
	v_rcp_f32_e32 v8, v8
	v_add_f32_e32 v9, 0x45fd2000, v13
	v_rcp_f32_e32 v9, v9
	v_mul_f32_e32 v12, v105, v101
	v_mul_f32_e32 v12, v8, v12
	v_mul_f32_e32 v8, v94, v86
	v_mul_f32_e32 v13, v9, v8
	v_fmamk_f32 v8, v95, 0xbc03513b, v201
	v_exp_f32_e32 v8, v8
	v_fmamk_f32 v9, v96, 0xbc03513b, v201
	v_exp_f32_e32 v9, v9
	v_fmamk_f32 v16, v97, 0xbc03513b, v201
	v_add_f32_e32 v8, 0x45fd2000, v8
	v_rcp_f32_e32 v8, v8
	v_add_f32_e32 v9, 0x45fd2000, v9
	v_rcp_f32_e32 v9, v9
	v_exp_f32_e32 v16, v16
	v_mul_f32_e32 v15, v95, v87
	v_mul_f32_e32 v15, v8, v15
	v_mul_f32_e32 v8, v96, v88
	v_mul_f32_e32 v17, v9, v8
	v_add_f32_e32 v8, 0x45fd2000, v16
	v_rcp_f32_e32 v16, v8
	v_mov_b32_e32 v9, 0
	v_cvt_pk_fp8_f32 v9, v13, v15
	v_mov_b32_e32 v8, 0
	v_cvt_pk_fp8_f32 v8, v7, v11
	v_mul_f32_e32 v7, v97, v89
	v_mul_f32_e32 v7, v16, v7
	v_cvt_pk_fp8_f32 v9, v17, v7 op_sel:[0,0,1]
	v_fmamk_f32 v7, v78, 0xbc03513b, v201
	v_exp_f32_e32 v7, v7
	v_cvt_pk_fp8_f32 v8, v14, v12 op_sel:[0,0,1]
	v_or_b32_e32 v10, 48, v6
	v_mad_i64_i32 v[10:11], s[44:45], v10, s65, v[4:5]
	v_add_f32_e32 v7, 0x45fd2000, v7
	v_rcp_f32_e32 v7, v7
	v_lshl_add_u64 v[10:11], v[10:11], 0, v[2:3]
	global_store_dwordx2 v[10:11], v[8:9], off
	v_fmamk_f32 v8, v79, 0xbc03513b, v201
	v_mul_f32_e32 v9, v78, v90
	v_exp_f32_e32 v8, v8
	v_mul_f32_e32 v7, v7, v9
	v_fmamk_f32 v9, v80, 0xbc03513b, v201
	v_exp_f32_e32 v9, v9
	v_add_f32_e32 v8, 0x45fd2000, v8
	v_rcp_f32_e32 v8, v8
	v_fmamk_f32 v12, v81, 0xbc03513b, v201
	v_add_f32_e32 v9, 0x45fd2000, v9
	v_rcp_f32_e32 v9, v9
	v_exp_f32_e32 v12, v12
	v_fmamk_f32 v13, v70, 0xbc03513b, v201
	v_exp_f32_e32 v13, v13
	v_mul_f32_e32 v11, v79, v91
	v_mul_f32_e32 v11, v8, v11
	v_mul_f32_e32 v8, v80, v92
	v_mul_f32_e32 v14, v9, v8
	v_add_f32_e32 v8, 0x45fd2000, v12
	v_rcp_f32_e32 v8, v8
	v_add_f32_e32 v9, 0x45fd2000, v13
	v_rcp_f32_e32 v9, v9
	v_mul_f32_e32 v12, v81, v93
	v_mul_f32_e32 v12, v8, v12
	v_mul_f32_e32 v8, v70, v82
	v_mul_f32_e32 v13, v9, v8
	v_fmamk_f32 v8, v71, 0xbc03513b, v201
	v_exp_f32_e32 v8, v8
	v_fmamk_f32 v9, v72, 0xbc03513b, v201
	v_exp_f32_e32 v9, v9
	v_fmamk_f32 v16, v73, 0xbc03513b, v201
	v_add_f32_e32 v8, 0x45fd2000, v8
	v_rcp_f32_e32 v8, v8
	v_add_f32_e32 v9, 0x45fd2000, v9
	v_rcp_f32_e32 v9, v9
	v_exp_f32_e32 v16, v16
	v_mul_f32_e32 v15, v71, v83
	v_mul_f32_e32 v15, v8, v15
	v_mul_f32_e32 v8, v72, v84
	v_mul_f32_e32 v17, v9, v8
	v_add_f32_e32 v8, 0x45fd2000, v16
	v_rcp_f32_e32 v16, v8
	v_mov_b32_e32 v9, 0
	v_cvt_pk_fp8_f32 v9, v13, v15
	v_mov_b32_e32 v8, 0
	v_cvt_pk_fp8_f32 v8, v7, v11
	v_mul_f32_e32 v7, v73, v85
	v_mul_f32_e32 v7, v16, v7
	v_cvt_pk_fp8_f32 v9, v17, v7 op_sel:[0,0,1]
	v_fmamk_f32 v7, v58, 0xbc03513b, v201
	v_exp_f32_e32 v7, v7
	v_cvt_pk_fp8_f32 v8, v14, v12 op_sel:[0,0,1]
	v_add_u32_e32 v10, 0x80, v6
	v_mad_i64_i32 v[10:11], s[44:45], v10, s65, v[4:5]
	v_add_f32_e32 v7, 0x45fd2000, v7
	v_rcp_f32_e32 v7, v7
	v_lshl_add_u64 v[10:11], v[10:11], 0, v[2:3]
	global_store_dwordx2 v[10:11], v[8:9], off
	v_fmamk_f32 v8, v59, 0xbc03513b, v201
	v_mul_f32_e32 v9, v58, v74
	v_exp_f32_e32 v8, v8
	v_mul_f32_e32 v7, v7, v9
	v_fmamk_f32 v9, v60, 0xbc03513b, v201
	v_exp_f32_e32 v9, v9
	v_add_f32_e32 v8, 0x45fd2000, v8
	v_rcp_f32_e32 v8, v8
	v_fmamk_f32 v12, v61, 0xbc03513b, v201
	v_add_f32_e32 v9, 0x45fd2000, v9
	v_rcp_f32_e32 v9, v9
	v_exp_f32_e32 v12, v12
	v_fmamk_f32 v13, v50, 0xbc03513b, v201
	v_exp_f32_e32 v13, v13
	v_mul_f32_e32 v11, v59, v75
	v_mul_f32_e32 v11, v8, v11
	v_mul_f32_e32 v8, v60, v76
	v_mul_f32_e32 v14, v9, v8
	v_add_f32_e32 v8, 0x45fd2000, v12
	v_rcp_f32_e32 v8, v8
	v_add_f32_e32 v9, 0x45fd2000, v13
	v_rcp_f32_e32 v9, v9
	v_mul_f32_e32 v12, v61, v77
	v_mul_f32_e32 v12, v8, v12
	v_mul_f32_e32 v8, v50, v66
	v_mul_f32_e32 v13, v9, v8
	v_fmamk_f32 v8, v51, 0xbc03513b, v201
	v_exp_f32_e32 v8, v8
	v_fmamk_f32 v9, v52, 0xbc03513b, v201
	v_exp_f32_e32 v9, v9
	v_fmamk_f32 v16, v53, 0xbc03513b, v201
	v_add_f32_e32 v8, 0x45fd2000, v8
	v_rcp_f32_e32 v8, v8
	v_add_f32_e32 v9, 0x45fd2000, v9
	v_rcp_f32_e32 v9, v9
	v_exp_f32_e32 v16, v16
	v_mul_f32_e32 v15, v51, v67
	v_mul_f32_e32 v15, v8, v15
;     __device__ __forceinline__ void operator()(const Acc& acc, const Unit& u, int wr, int wc, int fr, int fq) const {
;     ...
;         for (int ai = 0; ai < 2; ++ai)
; #pragma unroll
;             for (int m = 0; m < 4; ++m) { const size_t off = (size_t)(row0 + ai * HALF + m * 16) * ldc + col0;
;                 float h[8];
; #pragma unroll
;                 for (int n = 0; n < 2; ++n)
; #pragma unroll
;                     for (int e = 0; e < 4; ++e) { const float a0 = acc[ai][0][m][n][e], a1 = acc[ai][1][m][n][e];
;                         h[n * 4 + e] = (a0 * a1) * __builtin_amdgcn_rcpf(c3 + __builtin_amdgcn_exp2f(fmaf(a0, c1, c0))); }
;                 if constexpr (FP8OUT == 2) { u32x2 w; w.x = pk4_i8(h[0], h[1], h[2], h[3]); w.y = pk4_i8(h[4], h[5], h[6], h[7]); *(u32x2*)((unsigned char*)H + off) = w; }
;                 else if constexpr (FP8OUT == 1) { u32x2 w; w.x = pk4_fp8_nc(h[0], h[1], h[2], h[3]); w.y = pk4_fp8_nc(h[4], h[5], h[6], h[7]); *(u32x2*)((unsigned char*)H + off) = w; }
	v_mul_f32_e32 v8, v52, v68
	v_mul_f32_e32 v17, v9, v8
	v_add_f32_e32 v8, 0x45fd2000, v16
	v_rcp_f32_e32 v16, v8
	v_mov_b32_e32 v9, 0
	v_cvt_pk_fp8_f32 v9, v13, v15
	v_mov_b32_e32 v8, 0
	v_cvt_pk_fp8_f32 v8, v7, v11
	v_mul_f32_e32 v7, v53, v69
	v_mul_f32_e32 v7, v16, v7
	v_cvt_pk_fp8_f32 v9, v17, v7 op_sel:[0,0,1]
	v_fmamk_f32 v7, v42, 0xbc03513b, v201
	v_exp_f32_e32 v7, v7
	v_cvt_pk_fp8_f32 v8, v14, v12 op_sel:[0,0,1]
	v_add_u32_e32 v10, 0x90, v6
	v_mad_i64_i32 v[10:11], s[44:45], v10, s65, v[4:5]
	v_add_f32_e32 v7, 0x45fd2000, v7
	v_rcp_f32_e32 v7, v7
	v_lshl_add_u64 v[10:11], v[10:11], 0, v[2:3]
	global_store_dwordx2 v[10:11], v[8:9], off
	v_fmamk_f32 v8, v43, 0xbc03513b, v201
	v_mul_f32_e32 v9, v42, v62
	v_exp_f32_e32 v8, v8
	v_mul_f32_e32 v7, v7, v9
	v_fmamk_f32 v9, v44, 0xbc03513b, v201
	v_exp_f32_e32 v9, v9
	v_add_f32_e32 v8, 0x45fd2000, v8
	v_rcp_f32_e32 v8, v8
	v_fmamk_f32 v12, v45, 0xbc03513b, v201
	v_add_f32_e32 v9, 0x45fd2000, v9
	v_rcp_f32_e32 v9, v9
	v_exp_f32_e32 v12, v12
	v_fmamk_f32 v13, v34, 0xbc03513b, v201
	v_exp_f32_e32 v13, v13
	v_mul_f32_e32 v11, v43, v63
	v_mul_f32_e32 v11, v8, v11
	v_mul_f32_e32 v8, v44, v64
	v_mul_f32_e32 v14, v9, v8
	v_add_f32_e32 v8, 0x45fd2000, v12
	v_rcp_f32_e32 v8, v8
	v_add_f32_e32 v9, 0x45fd2000, v13
	v_rcp_f32_e32 v9, v9
	v_mul_f32_e32 v12, v45, v65
	v_mul_f32_e32 v12, v8, v12
	v_mul_f32_e32 v8, v34, v54
	v_mul_f32_e32 v13, v9, v8
	v_fmamk_f32 v8, v35, 0xbc03513b, v201
	v_exp_f32_e32 v8, v8
	v_fmamk_f32 v9, v36, 0xbc03513b, v201
	v_exp_f32_e32 v9, v9
	v_fmamk_f32 v16, v37, 0xbc03513b, v201
	v_add_f32_e32 v8, 0x45fd2000, v8
	v_rcp_f32_e32 v8, v8
	v_add_f32_e32 v9, 0x45fd2000, v9
	v_rcp_f32_e32 v9, v9
	v_exp_f32_e32 v16, v16
	v_mul_f32_e32 v15, v35, v55
	v_mul_f32_e32 v15, v8, v15
	v_mul_f32_e32 v8, v36, v56
	v_mul_f32_e32 v17, v9, v8
	v_add_f32_e32 v8, 0x45fd2000, v16
	v_rcp_f32_e32 v16, v8
	v_mov_b32_e32 v9, 0
	v_mov_b32_e32 v8, 0
	v_cvt_pk_fp8_f32 v9, v13, v15
	v_cvt_pk_fp8_f32 v8, v7, v11
	v_mul_f32_e32 v7, v37, v57
	v_mul_f32_e32 v7, v16, v7
	v_cvt_pk_fp8_f32 v9, v17, v7 op_sel:[0,0,1]
	v_fmamk_f32 v7, v30, 0xbc03513b, v201
	v_cvt_pk_fp8_f32 v8, v14, v12 op_sel:[0,0,1]
	v_exp_f32_e32 v7, v7
	v_add_u32_e32 v10, 0xa0, v6
	v_mad_i64_i32 v[10:11], s[44:45], v10, s65, v[4:5]
	v_lshl_add_u64 v[10:11], v[10:11], 0, v[2:3]
	global_store_dwordx2 v[10:11], v[8:9], off
	v_add_f32_e32 v7, 0x45fd2000, v7
	v_fmamk_f32 v8, v31, 0xbc03513b, v201
	v_rcp_f32_e32 v7, v7
	v_exp_f32_e32 v8, v8
	v_add_u32_e32 v9, 0xb0, v6
	v_mul_f32_e32 v6, v30, v46
	v_mul_f32_e32 v7, v7, v6
	v_add_f32_e32 v6, 0x45fd2000, v8
	v_fmamk_f32 v8, v32, 0xbc03513b, v201
	v_exp_f32_e32 v8, v8
	v_rcp_f32_e32 v6, v6
	v_fmamk_f32 v11, v33, 0xbc03513b, v201
	v_exp_f32_e32 v11, v11
	v_add_f32_e32 v8, 0x45fd2000, v8
	v_rcp_f32_e32 v8, v8
	v_fmamk_f32 v12, v26, 0xbc03513b, v201
	v_exp_f32_e32 v12, v12
	v_mul_f32_e32 v10, v31, v47
	v_mul_f32_e32 v10, v6, v10
	v_mul_f32_e32 v6, v32, v48
	v_mul_f32_e32 v8, v8, v6
	v_add_f32_e32 v6, 0x45fd2000, v11
	v_rcp_f32_e32 v6, v6
	v_add_f32_e32 v11, 0x45fd2000, v12
	v_rcp_f32_e32 v11, v11
	v_mul_f32_e32 v12, v33, v49
	v_mul_f32_e32 v12, v6, v12
	v_mul_f32_e32 v6, v26, v38
	v_mul_f32_e32 v11, v11, v6
	v_fmamk_f32 v6, v27, 0xbc03513b, v201
	v_exp_f32_e32 v6, v6
	v_fmamk_f32 v13, v28, 0xbc03513b, v201
	v_exp_f32_e32 v13, v13
	v_fmamk_f32 v15, v29, 0xbc03513b, v201
	v_add_f32_e32 v6, 0x45fd2000, v6
	v_rcp_f32_e32 v6, v6
	v_add_f32_e32 v13, 0x45fd2000, v13
	v_rcp_f32_e32 v13, v13
	v_exp_f32_e32 v15, v15
	v_mul_f32_e32 v14, v27, v39
	v_mul_f32_e32 v14, v6, v14
	v_mul_f32_e32 v6, v28, v40
	v_mul_f32_e32 v13, v13, v6
	v_add_f32_e32 v6, 0x45fd2000, v15
	v_rcp_f32_e32 v15, v6
	v_mov_b32_e32 v6, 0
	v_cvt_pk_fp8_f32 v6, v7, v10
	v_mov_b32_e32 v7, 0
	v_cvt_pk_fp8_f32 v7, v11, v14
	v_mul_f32_e32 v10, v29, v41
	v_mul_f32_e32 v10, v15, v10
	v_cvt_pk_fp8_f32 v6, v8, v12 op_sel:[0,0,1]
	v_cvt_pk_fp8_f32 v7, v13, v10 op_sel:[0,0,1]
	v_mad_i64_i32 v[4:5], s[44:45], v9, s65, v[4:5]
	v_lshl_add_u64 v[2:3], v[4:5], 0, v[2:3]
	s_cmp_lt_u32 s98, 28
	s_cbranch_scc0 .Lmd_nostore
;     __device__ __forceinline__ bool next(int i, Unit& u) const { if (!T.tile(i, u.pm, u.pn)) return false; u.aoff = (size_t)u.pm * atile; u.boff = (size_t)u.pn * btile; return true; }
;     __device__ __forceinline__ bool next(int i, Unit& u) const { if (!T.tile(i, u.pm, u.pn)) return false; u.aoff = (size_t)u.pm * 256 * D * 2 + (size_t)(u.pn >> 1) * 512; u.boff = (size_t)u.pn * 256 * 256 * 2; return true; }
;     __device__ __forceinline__ bool next(int i, Unit& u) const { if (!T.tile(i, u.pm, u.pn)) return false; const int e = tile_e[u.pm] & 7; u.aoff = (size_t)u.pm * atile; u.boff = ((size_t)e * nN + u.pn) * btile; return true; }
; __device__ __forceinline__ void cvt_store(CvtState& cs, int lane, const f32x4 (&v)[8]) {
;     const int kb = cs.next % CV_KB, tmp = cs.next / CV_KB, nb = tmp % CV_NB, e = tmp / CV_NB;
;     unsigned char* dst = cs.WT + ((size_t)e * D + (size_t)(16 * nb + 4 * (lane & 3))) * FF + 128 * kb + 8 * (lane >> 2);
; #pragma unroll
;     for (int j = 0; j < 4; ++j) { u32x2 w; w.x = pk4_fp8(v[0][j] * CV_WS, v[1][j] * CV_WS, v[2][j] * CV_WS, v[3][j] * CV_WS); w.y = pk4_fp8(v[4][j] * CV_WS, v[5][j] * CV_WS, v[6][j] * CV_WS, v[7][j] * CV_WS);
;         *(u32x2*)(dst + (size_t)j * FF) = w; }
;     ++cs.next;
	s_waitcnt vmcnt(7)
	s_lshl_b32 s100, s98, 7
	v_lshl_add_u64 v[240:241], s[100:101], 0, v[246:247]
	v_mul_f32_e32 v202, 0x42800000, v202
	v_mul_f32_e32 v206, 0x42800000, v206
	v_mul_f32_e32 v210, 0x42800000, v210
	v_mul_f32_e32 v214, 0x42800000, v214
	v_mul_f32_e32 v218, 0x42800000, v218
	v_mul_f32_e32 v222, 0x42800000, v222
	v_mul_f32_e32 v226, 0x42800000, v226
	v_mul_f32_e32 v230, 0x42800000, v230
	v_med3_f32 v202, v202, v249, v248
	v_med3_f32 v206, v206, v249, v248
	v_med3_f32 v210, v210, v249, v248
	v_med3_f32 v214, v214, v249, v248
	v_med3_f32 v218, v218, v249, v248
	v_med3_f32 v222, v222, v249, v248
	v_med3_f32 v226, v226, v249, v248
	v_med3_f32 v230, v230, v249, v248
	v_mov_b32_e32 v238, 0
	v_mov_b32_e32 v239, 0
	v_cvt_pk_fp8_f32 v238, v202, v206
	v_cvt_pk_fp8_f32 v239, v218, v222
	v_cvt_pk_fp8_f32 v238, v210, v214 op_sel:[0,0,1]
	v_cvt_pk_fp8_f32 v239, v226, v230 op_sel:[0,0,1]
	s_nop 0
	global_store_dwordx2 v[240:241], v[238:239], off
	v_mul_f32_e32 v203, 0x42800000, v203
	v_mul_f32_e32 v207, 0x42800000, v207
	v_mul_f32_e32 v211, 0x42800000, v211
	v_mul_f32_e32 v215, 0x42800000, v215
	v_mul_f32_e32 v219, 0x42800000, v219
	v_mul_f32_e32 v223, 0x42800000, v223
	v_mul_f32_e32 v227, 0x42800000, v227
	v_mul_f32_e32 v231, 0x42800000, v231
	v_med3_f32 v203, v203, v249, v248
	v_med3_f32 v207, v207, v249, v248
	v_med3_f32 v211, v211, v249, v248
	v_med3_f32 v215, v215, v249, v248
	v_med3_f32 v219, v219, v249, v248
	v_med3_f32 v223, v223, v249, v248
	v_med3_f32 v227, v227, v249, v248
	v_med3_f32 v231, v231, v249, v248
	v_mov_b32_e32 v238, 0
	v_mov_b32_e32 v239, 0
	v_cvt_pk_fp8_f32 v238, v203, v207
	v_cvt_pk_fp8_f32 v239, v219, v223
	v_cvt_pk_fp8_f32 v238, v211, v215 op_sel:[0,0,1]
	v_cvt_pk_fp8_f32 v239, v227, v231 op_sel:[0,0,1]
	s_mov_b32 s100, 0x1c00
	v_lshl_add_u64 v[242:243], s[100:101], 0, v[240:241]
	global_store_dwordx2 v[242:243], v[238:239], off
	v_mul_f32_e32 v204, 0x42800000, v204
	v_mul_f32_e32 v208, 0x42800000, v208
	v_mul_f32_e32 v212, 0x42800000, v212
	v_mul_f32_e32 v216, 0x42800000, v216
	v_mul_f32_e32 v220, 0x42800000, v220
	v_mul_f32_e32 v224, 0x42800000, v224
	v_mul_f32_e32 v228, 0x42800000, v228
	v_mul_f32_e32 v232, 0x42800000, v232
	v_med3_f32 v204, v204, v249, v248
	v_med3_f32 v208, v208, v249, v248
	v_med3_f32 v212, v212, v249, v248
	v_med3_f32 v216, v216, v249, v248
	v_med3_f32 v220, v220, v249, v248
	v_med3_f32 v224, v224, v249, v248
	v_med3_f32 v228, v228, v249, v248
	v_med3_f32 v232, v232, v249, v248
	v_mov_b32_e32 v238, 0
	v_mov_b32_e32 v239, 0
	v_cvt_pk_fp8_f32 v238, v204, v208
	v_cvt_pk_fp8_f32 v239, v220, v224
	v_cvt_pk_fp8_f32 v238, v212, v216 op_sel:[0,0,1]
	v_cvt_pk_fp8_f32 v239, v228, v232 op_sel:[0,0,1]
	s_mov_b32 s100, 0x3800
	v_lshl_add_u64 v[242:243], s[100:101], 0, v[240:241]
	global_store_dwordx2 v[242:243], v[238:239], off
	v_mul_f32_e32 v205, 0x42800000, v205
	v_mul_f32_e32 v209, 0x42800000, v209
	v_mul_f32_e32 v213, 0x42800000, v213
	v_mul_f32_e32 v217, 0x42800000, v217
	v_mul_f32_e32 v221, 0x42800000, v221
	v_mul_f32_e32 v225, 0x42800000, v225
	v_mul_f32_e32 v229, 0x42800000, v229
	v_mul_f32_e32 v233, 0x42800000, v233
	v_med3_f32 v205, v205, v249, v248
	v_med3_f32 v209, v209, v249, v248
	v_med3_f32 v213, v213, v249, v248
	v_med3_f32 v217, v217, v249, v248
	v_med3_f32 v221, v221, v249, v248
	v_med3_f32 v225, v225, v249, v248
	v_med3_f32 v229, v229, v249, v248
	v_med3_f32 v233, v233, v249, v248
	v_mov_b32_e32 v238, 0
	v_mov_b32_e32 v239, 0
	v_cvt_pk_fp8_f32 v238, v205, v209
	v_cvt_pk_fp8_f32 v239, v221, v225
	v_cvt_pk_fp8_f32 v238, v213, v217 op_sel:[0,0,1]
	v_cvt_pk_fp8_f32 v239, v229, v233 op_sel:[0,0,1]
	s_mov_b32 s100, 0x5400
	v_lshl_add_u64 v[242:243], s[100:101], 0, v[240:241]
	global_store_dwordx2 v[242:243], v[238:239], off
	s_add_u32 s98, s98, 1
.Lmd_nostore:
	s_andn2_b64 vcc, exec, s[4:5]
	s_mov_b64 s[4:5], -1
	global_store_dwordx2 v[2:3], v[6:7], off
	s_cbranch_vccnz .LBB0_1405
	s_andn2_b64 vcc, exec, s[14:15]
	s_cbranch_vccnz .LBB0_1404
	s_barrier
	s_branch .LBB0_1404

; __device__ __forceinline__ int opaque_tid() { int t = threadIdx.x; asm volatile("" : "+v"(t)); return t; }
;     __device__ __forceinline__ bool next(int i, Unit& u) const { if (!T.tile(i, u.pm, u.pn)) return false; u.aoff = (size_t)u.pm * atile; u.boff = (size_t)u.pn * btile; return true; }
;     __device__ __forceinline__ bool next(int i, Unit& u) const { if (!T.tile(i, u.pm, u.pn)) return false; u.aoff = (size_t)u.pm * 256 * D * 2 + (size_t)(u.pn >> 1) * 512; u.boff = (size_t)u.pn * 256 * 256 * 2; return true; }
;     __device__ __forceinline__ bool next(int i, Unit& u) const { if (!T.tile(i, u.pm, u.pn)) return false; const int e = tile_e[u.pm] & 7; u.aoff = (size_t)u.pm * atile; u.boff = ((size_t)e * nN + u.pn) * btile; return true; }
; __device__ __forceinline__ void cvt_load(const CvtState& cs, int lane, f32x4 (&v)[8]) {
;     const int kb = cs.next % CV_KB, tmp = cs.next / CV_KB, nb = tmp % CV_NB, e = tmp / CV_NB;
;     const float* src = cs.W + ((size_t)e * FF + (size_t)(128 * kb + 8 * (lane >> 2))) * D + 16 * nb + 4 * (lane & 3);
; #pragma unroll
;     for (int i = 0; i < 8; ++i) v[i] = *(const f32x4*)(src + (size_t)i * D);
; }
; __device__ __forceinline__ void cvt_store(CvtState& cs, int lane, const f32x4 (&v)[8]) {
;     const int kb = cs.next % CV_KB, tmp = cs.next / CV_KB, nb = tmp % CV_NB, e = tmp / CV_NB;
;     unsigned char* dst = cs.WT + ((size_t)e * D + (size_t)(16 * nb + 4 * (lane & 3))) * FF + 128 * kb + 8 * (lane >> 2);
; #pragma unroll
;     for (int j = 0; j < 4; ++j) { u32x2 w; w.x = pk4_fp8(v[0][j] * CV_WS, v[1][j] * CV_WS, v[2][j] * CV_WS, v[3][j] * CV_WS); w.y = pk4_fp8(v[4][j] * CV_WS, v[5][j] * CV_WS, v[6][j] * CV_WS, v[7][j] * CV_WS);
;         *(u32x2*)(dst + (size_t)j * FF) = w; }
;     ++cs.next;
; __global__ void __launch_bounds__(NTHREADS, 2) fwd_kernel(Args args) {
;     ...
;         { const int lane_ = opaque_tid() & 63;
; #pragma nounroll
;           while (cs.next < cs.end) { f32x4 cv[8]; att::cvt_load(cs, lane_, cv); att::cvt_store(cs, lane_, cv); } }
.LBB0_1416:
.Lmd_fb_top:
	s_cmp_lt_u32 s98, 28
	s_cbranch_scc0 .Lmd_fb_done
	s_lshl_b32 s100, s98, 20
	v_lshl_add_u64 v[234:235], s[100:101], 0, v[244:245]
	global_load_dwordx4 v[202:205], v[234:235], off
	s_mov_b32 s100, 0x2000
	v_lshl_add_u64 v[236:237], s[100:101], 0, v[234:235]
	global_load_dwordx4 v[206:209], v[236:237], off
	s_mov_b32 s100, 0x4000
	v_lshl_add_u64 v[236:237], s[100:101], 0, v[234:235]
	global_load_dwordx4 v[210:213], v[236:237], off
	s_mov_b32 s100, 0x6000
	v_lshl_add_u64 v[236:237], s[100:101], 0, v[234:235]
	global_load_dwordx4 v[214:217], v[236:237], off
	s_mov_b32 s100, 0x8000
	v_lshl_add_u64 v[236:237], s[100:101], 0, v[234:235]
	global_load_dwordx4 v[218:221], v[236:237], off
	s_mov_b32 s100, 0xa000
	v_lshl_add_u64 v[236:237], s[100:101], 0, v[234:235]
	global_load_dwordx4 v[222:225], v[236:237], off
	s_mov_b32 s100, 0xc000
	v_lshl_add_u64 v[236:237], s[100:101], 0, v[234:235]
	global_load_dwordx4 v[226:229], v[236:237], off
	s_mov_b32 s100, 0xe000
	v_lshl_add_u64 v[236:237], s[100:101], 0, v[234:235]
	global_load_dwordx4 v[230:233], v[236:237], off
	s_waitcnt vmcnt(0)
	s_lshl_b32 s100, s98, 7
	v_lshl_add_u64 v[240:241], s[100:101], 0, v[246:247]
	v_mul_f32_e32 v202, 0x42800000, v202
	v_mul_f32_e32 v206, 0x42800000, v206
	v_mul_f32_e32 v210, 0x42800000, v210
	v_mul_f32_e32 v214, 0x42800000, v214
	v_mul_f32_e32 v218, 0x42800000, v218
	v_mul_f32_e32 v222, 0x42800000, v222
	v_mul_f32_e32 v226, 0x42800000, v226
	v_mul_f32_e32 v230, 0x42800000, v230
	v_med3_f32 v202, v202, v249, v248
	v_med3_f32 v206, v206, v249, v248
	v_med3_f32 v210, v210, v249, v248
	v_med3_f32 v214, v214, v249, v248
	v_med3_f32 v218, v218, v249, v248
	v_med3_f32 v222, v222, v249, v248
	v_med3_f32 v226, v226, v249, v248
	v_med3_f32 v230, v230, v249, v248
	v_mov_b32_e32 v238, 0
	v_mov_b32_e32 v239, 0
	v_cvt_pk_fp8_f32 v238, v202, v206
	v_cvt_pk_fp8_f32 v239, v218, v222
	v_cvt_pk_fp8_f32 v238, v210, v214 op_sel:[0,0,1]
	v_cvt_pk_fp8_f32 v239, v226, v230 op_sel:[0,0,1]
	s_nop 0
	global_store_dwordx2 v[240:241], v[238:239], off
	v_mul_f32_e32 v203, 0x42800000, v203
	v_mul_f32_e32 v207, 0x42800000, v207
	v_mul_f32_e32 v211, 0x42800000, v211
	v_mul_f32_e32 v215, 0x42800000, v215
	v_mul_f32_e32 v219, 0x42800000, v219
	v_mul_f32_e32 v223, 0x42800000, v223
	v_mul_f32_e32 v227, 0x42800000, v227
	v_mul_f32_e32 v231, 0x42800000, v231
	v_med3_f32 v203, v203, v249, v248
	v_med3_f32 v207, v207, v249, v248
	v_med3_f32 v211, v211, v249, v248
	v_med3_f32 v215, v215, v249, v248
	v_med3_f32 v219, v219, v249, v248
	v_med3_f32 v223, v223, v249, v248
	v_med3_f32 v227, v227, v249, v248
	v_med3_f32 v231, v231, v249, v248
	v_mov_b32_e32 v238, 0
	v_mov_b32_e32 v239, 0
	v_cvt_pk_fp8_f32 v238, v203, v207
	v_cvt_pk_fp8_f32 v239, v219, v223
	v_cvt_pk_fp8_f32 v238, v211, v215 op_sel:[0,0,1]
	v_cvt_pk_fp8_f32 v239, v227, v231 op_sel:[0,0,1]
	s_mov_b32 s100, 0x1c00
	v_lshl_add_u64 v[242:243], s[100:101], 0, v[240:241]
	global_store_dwordx2 v[242:243], v[238:239], off
	v_mul_f32_e32 v204, 0x42800000, v204
	v_mul_f32_e32 v208, 0x42800000, v208
	v_mul_f32_e32 v212, 0x42800000, v212
	v_mul_f32_e32 v216, 0x42800000, v216
	v_mul_f32_e32 v220, 0x42800000, v220
	v_mul_f32_e32 v224, 0x42800000, v224
	v_mul_f32_e32 v228, 0x42800000, v228
	v_mul_f32_e32 v232, 0x42800000, v232
	v_med3_f32 v204, v204, v249, v248
	v_med3_f32 v208, v208, v249, v248
	v_med3_f32 v212, v212, v249, v248
	v_med3_f32 v216, v216, v249, v248
	v_med3_f32 v220, v220, v249, v248
	v_med3_f32 v224, v224, v249, v248
	v_med3_f32 v228, v228, v249, v248
	v_med3_f32 v232, v232, v249, v248
	v_mov_b32_e32 v238, 0
	v_mov_b32_e32 v239, 0
	v_cvt_pk_fp8_f32 v238, v204, v208
	v_cvt_pk_fp8_f32 v239, v220, v224
	v_cvt_pk_fp8_f32 v238, v212, v216 op_sel:[0,0,1]
	v_cvt_pk_fp8_f32 v239, v228, v232 op_sel:[0,0,1]
	s_mov_b32 s100, 0x3800
	v_lshl_add_u64 v[242:243], s[100:101], 0, v[240:241]
	global_store_dwordx2 v[242:243], v[238:239], off
	v_mul_f32_e32 v205, 0x42800000, v205
	v_mul_f32_e32 v209, 0x42800000, v209
	v_mul_f32_e32 v213, 0x42800000, v213
	v_mul_f32_e32 v217, 0x42800000, v217
	v_mul_f32_e32 v221, 0x42800000, v221
	v_mul_f32_e32 v225, 0x42800000, v225
	v_mul_f32_e32 v229, 0x42800000, v229
	v_mul_f32_e32 v233, 0x42800000, v233
	v_med3_f32 v205, v205, v249, v248
	v_med3_f32 v209, v209, v249, v248
	v_med3_f32 v213, v213, v249, v248
	v_med3_f32 v217, v217, v249, v248
	v_med3_f32 v221, v221, v249, v248
	v_med3_f32 v225, v225, v249, v248
	v_med3_f32 v229, v229, v249, v248
	v_med3_f32 v233, v233, v249, v248
	v_mov_b32_e32 v238, 0
	v_mov_b32_e32 v239, 0
	v_cvt_pk_fp8_f32 v238, v205, v209
	v_cvt_pk_fp8_f32 v239, v221, v225
	v_cvt_pk_fp8_f32 v238, v213, v217 op_sel:[0,0,1]
	v_cvt_pk_fp8_f32 v239, v229, v233 op_sel:[0,0,1]
	s_mov_b32 s100, 0x5400
	v_lshl_add_u64 v[242:243], s[100:101], 0, v[240:241]
	global_store_dwordx2 v[242:243], v[238:239], off
	s_add_u32 s98, s98, 1
	s_branch .Lmd_fb_top
